# GEMM accumulator re-zeroing between units: 64-bit moves of constant 0 instead of 127 single-dword copies (all six GEMM phases)
# speedup vs baseline: 1.0123x; 1.0002x over previous
; template <class Epi, class Sched, bool ALIGN_EPI, bool SP2, bool FP8 = false>
; __device__ __forceinline__ void gemm_phase(LAS unsigned char* lds, const int K, const Sched& S, const Epi& E) {
;     ...
; #pragma unroll
;         for (int a = 0; a < 2; ++a)
; #pragma unroll
;             for (int b = 0; b < 2; ++b)
; #pragma unroll
;                 for (int m = 0; m < 4; ++m)
; #pragma unroll
;                     for (int n = 0; n < 2; ++n) acc[a][b][m][n] = (f32x4){0.f, 0.f, 0.f, 0.f};
;         cur = nxt; cA = nA; cB = nB; ++ui;
; #pragma unroll
;         for (int h = 0; h < 2; ++h)
; #pragma unroll
;             for (int i = 0; i < 2; ++i) vAc[h][i] = vAn[h][i];
.LBB0_202:
	s_add_u32 s70, s4, 0x80
	s_addc_u32 s71, s5, 0
	v_mov_b32_e32 v143, v137
	v_mov_b32_e32 v147, v137
	s_add_u32 s45, s68, 0x100
	v_mov_b32_e32 v82, 0
	v_lshl_add_u64 v[150:151], s[70:71], 0, v[146:147]
	v_lshl_add_u64 v[152:153], s[70:71], 0, v[142:143]
	s_addc_u32 s96, s69, 0
	s_mov_b32 s97, -2
	s_mov_b64 s[68:69], 0
	v_mov_b64_e32 v[2:3], 0
	v_mov_b64_e32 v[4:5], 0
	v_mov_b64_e32 v[6:7], 0
	v_mov_b64_e32 v[8:9], 0
	v_mov_b64_e32 v[10:11], 0
	v_mov_b64_e32 v[12:13], 0
	v_mov_b64_e32 v[14:15], 0
	v_mov_b64_e32 v[16:17], 0
	v_mov_b64_e32 v[18:19], 0
	v_mov_b64_e32 v[20:21], 0
	v_mov_b64_e32 v[22:23], 0
	v_mov_b64_e32 v[24:25], 0
	v_mov_b64_e32 v[26:27], 0
	v_mov_b64_e32 v[28:29], 0
	v_mov_b64_e32 v[30:31], 0
	v_mov_b64_e32 v[32:33], 0
	v_mov_b64_e32 v[34:35], 0
	v_mov_b64_e32 v[36:37], 0
	v_mov_b64_e32 v[38:39], 0
	v_mov_b64_e32 v[40:41], 0
	v_mov_b64_e32 v[42:43], 0
	v_mov_b64_e32 v[44:45], 0
	v_mov_b64_e32 v[46:47], 0
	v_mov_b64_e32 v[48:49], 0
	v_mov_b64_e32 v[50:51], 0
	v_mov_b64_e32 v[52:53], 0
	v_mov_b64_e32 v[54:55], 0
	v_mov_b64_e32 v[56:57], 0
	v_mov_b64_e32 v[58:59], 0
	v_mov_b64_e32 v[60:61], 0
	v_mov_b64_e32 v[62:63], 0
	v_mov_b64_e32 v[64:65], 0
	v_mov_b64_e32 v[66:67], 0
	v_mov_b64_e32 v[68:69], 0
	v_mov_b64_e32 v[70:71], 0
	v_mov_b64_e32 v[72:73], 0
	v_mov_b64_e32 v[74:75], 0
	v_mov_b64_e32 v[76:77], 0
	v_mov_b64_e32 v[78:79], 0
	v_mov_b64_e32 v[80:81], 0
	v_mov_b32_e32 v83, v82
	v_mov_b64_e32 v[84:85], 0
	v_mov_b64_e32 v[86:87], 0
	v_mov_b64_e32 v[88:89], 0
	v_mov_b64_e32 v[90:91], 0
	v_mov_b64_e32 v[92:93], 0
	v_mov_b64_e32 v[94:95], 0
	v_mov_b64_e32 v[96:97], 0
	v_mov_b64_e32 v[98:99], 0
	v_mov_b64_e32 v[100:101], 0
	v_mov_b64_e32 v[102:103], 0
	v_mov_b64_e32 v[104:105], 0
	v_mov_b64_e32 v[106:107], 0
	v_mov_b64_e32 v[108:109], 0
	v_mov_b64_e32 v[110:111], 0
	v_mov_b64_e32 v[112:113], 0
	v_mov_b64_e32 v[114:115], 0
	v_mov_b64_e32 v[116:117], 0
	v_mov_b64_e32 v[118:119], 0
	v_mov_b64_e32 v[120:121], 0
	v_mov_b64_e32 v[122:123], 0
	v_mov_b64_e32 v[124:125], 0
	v_mov_b64_e32 v[126:127], 0
	v_mov_b64_e32 v[128:129], 0
	s_waitcnt vmcnt(0)
	s_waitcnt lgkmcnt(0)

; template <class Epi, class Sched, bool ALIGN_EPI, bool SP2, bool FP8 = false>
; __device__ __forceinline__ void gemm_phase(LAS unsigned char* lds, const int K, const Sched& S, const Epi& E) {
;     ...
; #pragma unroll
;         for (int a = 0; a < 2; ++a)
; #pragma unroll
;             for (int b = 0; b < 2; ++b)
; #pragma unroll
;                 for (int m = 0; m < 4; ++m)
; #pragma unroll
;                     for (int n = 0; n < 2; ++n) acc[a][b][m][n] = (f32x4){0.f, 0.f, 0.f, 0.f};
;         cur = nxt; cA = nA; cB = nB; ++ui;
; #pragma unroll
;         for (int h = 0; h < 2; ++h)
; #pragma unroll
;             for (int i = 0; i < 2; ++i) vAc[h][i] = vAn[h][i];
.LBB0_789:
	v_mov_b32_e32 v169, v167
	v_mov_b32_e32 v171, v167
	s_add_u32 s49, s58, 0x100
	v_mov_b32_e32 v66, 0
	v_lshl_add_u64 v[174:175], s[42:43], 0, v[170:171]
	v_lshl_add_u64 v[176:177], s[42:43], 0, v[168:169]
	s_addc_u32 s57, s59, 0
	s_mov_b32 s71, -2
	s_mov_b64 s[58:59], 0
	s_waitcnt lgkmcnt(0)
	v_mov_b64_e32 v[34:35], 0
	v_mov_b64_e32 v[36:37], 0
	v_mov_b64_e32 v[38:39], 0
	v_mov_b64_e32 v[40:41], 0
	v_mov_b64_e32 v[42:43], 0
	v_mov_b64_e32 v[44:45], 0
	v_mov_b64_e32 v[46:47], 0
	v_mov_b64_e32 v[48:49], 0
	v_mov_b64_e32 v[50:51], 0
	v_mov_b64_e32 v[52:53], 0
	v_mov_b64_e32 v[54:55], 0
	v_mov_b64_e32 v[56:57], 0
	v_mov_b64_e32 v[58:59], 0
	v_mov_b64_e32 v[60:61], 0
	v_mov_b64_e32 v[62:63], 0
	v_mov_b64_e32 v[64:65], 0
	v_mov_b32_e32 v67, v66
	v_mov_b64_e32 v[68:69], 0
	v_mov_b64_e32 v[70:71], 0
	v_mov_b64_e32 v[72:73], 0
	v_mov_b64_e32 v[74:75], 0
	v_mov_b64_e32 v[76:77], 0
	v_mov_b64_e32 v[78:79], 0
	v_mov_b64_e32 v[80:81], 0
	v_mov_b64_e32 v[82:83], 0
	v_mov_b64_e32 v[84:85], 0
	v_mov_b64_e32 v[86:87], 0
	v_mov_b64_e32 v[88:89], 0
	v_mov_b64_e32 v[90:91], 0
	v_mov_b64_e32 v[92:93], 0
	v_mov_b64_e32 v[94:95], 0
	v_mov_b64_e32 v[96:97], 0
	v_mov_b64_e32 v[98:99], 0
	v_mov_b64_e32 v[100:101], 0
	v_mov_b64_e32 v[102:103], 0
	v_mov_b64_e32 v[104:105], 0
	v_mov_b64_e32 v[106:107], 0
	v_mov_b64_e32 v[108:109], 0
	v_mov_b64_e32 v[110:111], 0
	v_mov_b64_e32 v[112:113], 0
	v_mov_b64_e32 v[114:115], 0
	v_mov_b64_e32 v[116:117], 0
	v_mov_b64_e32 v[118:119], 0
	v_mov_b64_e32 v[120:121], 0
	v_mov_b64_e32 v[122:123], 0
	v_mov_b64_e32 v[124:125], 0
	v_mov_b64_e32 v[126:127], 0
	v_mov_b64_e32 v[128:129], 0
	v_mov_b64_e32 v[130:131], 0
	v_mov_b64_e32 v[132:133], 0
	v_mov_b64_e32 v[134:135], 0
	v_mov_b64_e32 v[136:137], 0
	v_mov_b64_e32 v[138:139], 0
	v_mov_b64_e32 v[140:141], 0
	v_mov_b64_e32 v[142:143], 0
	v_mov_b64_e32 v[144:145], 0
	v_mov_b64_e32 v[146:147], 0
	v_mov_b64_e32 v[148:149], 0
	v_mov_b64_e32 v[150:151], 0
	v_mov_b64_e32 v[152:153], 0
	v_mov_b64_e32 v[154:155], 0
	v_mov_b64_e32 v[156:157], 0
	v_mov_b64_e32 v[158:159], 0
	v_mov_b64_e32 v[160:161], 0

; template <class Epi, class Sched, bool ALIGN_EPI, bool SP2, bool FP8 = false>
; __device__ __forceinline__ void gemm_phase(LAS unsigned char* lds, const int K, const Sched& S, const Epi& E) {
;     ...
; #pragma unroll
;         for (int a = 0; a < 2; ++a)
; #pragma unroll
;             for (int b = 0; b < 2; ++b)
; #pragma unroll
;                 for (int m = 0; m < 4; ++m)
; #pragma unroll
;                     for (int n = 0; n < 2; ++n) acc[a][b][m][n] = (f32x4){0.f, 0.f, 0.f, 0.f};
;         cur = nxt; cA = nA; cB = nB; ++ui;
; #pragma unroll
;         for (int h = 0; h < 2; ++h)
; #pragma unroll
;             for (int i = 0; i < 2; ++i) vAc[h][i] = vAn[h][i];
.LBB0_882:
	v_mov_b32_e32 v139, v137
	v_mov_b32_e32 v141, v137
	s_add_u32 s47, s4, 0x100
	v_mov_b32_e32 v26, 0
	v_lshl_add_u64 v[144:145], s[42:43], 0, v[140:141]
	v_lshl_add_u64 v[146:147], s[42:43], 0, v[138:139]
	s_addc_u32 s68, s5, 0
	s_mov_b32 s69, -2
	s_mov_b64 s[4:5], 0
	v_mov_b64_e32 v[2:3], 0
	v_mov_b64_e32 v[4:5], 0
	v_mov_b64_e32 v[6:7], 0
	v_mov_b64_e32 v[8:9], 0
	v_mov_b64_e32 v[10:11], 0
	v_mov_b64_e32 v[12:13], 0
	v_mov_b64_e32 v[14:15], 0
	v_mov_b64_e32 v[16:17], 0
	v_mov_b64_e32 v[18:19], 0
	v_mov_b64_e32 v[20:21], 0
	v_mov_b64_e32 v[22:23], 0
	v_mov_b64_e32 v[24:25], 0
	v_mov_b32_e32 v27, v26
	v_mov_b64_e32 v[28:29], 0
	v_mov_b64_e32 v[30:31], 0
	v_mov_b64_e32 v[32:33], 0
	v_mov_b64_e32 v[34:35], 0
	v_mov_b64_e32 v[36:37], 0
	v_mov_b64_e32 v[38:39], 0
	v_mov_b64_e32 v[40:41], 0
	v_mov_b64_e32 v[42:43], 0
	v_mov_b64_e32 v[44:45], 0
	v_mov_b64_e32 v[46:47], 0
	v_mov_b64_e32 v[48:49], 0
	v_mov_b64_e32 v[50:51], 0
	v_mov_b64_e32 v[52:53], 0
	v_mov_b64_e32 v[54:55], 0
	v_mov_b64_e32 v[56:57], 0
	v_mov_b64_e32 v[58:59], 0
	v_mov_b64_e32 v[60:61], 0
	v_mov_b64_e32 v[62:63], 0
	v_mov_b64_e32 v[64:65], 0
	v_mov_b64_e32 v[66:67], 0
	v_mov_b64_e32 v[68:69], 0
	v_mov_b64_e32 v[70:71], 0
	v_mov_b64_e32 v[72:73], 0
	v_mov_b64_e32 v[74:75], 0
	v_mov_b64_e32 v[76:77], 0
	v_mov_b64_e32 v[78:79], 0
	v_mov_b64_e32 v[80:81], 0
	v_mov_b64_e32 v[82:83], 0
	v_mov_b64_e32 v[84:85], 0
	v_mov_b64_e32 v[86:87], 0
	v_mov_b64_e32 v[88:89], 0
	v_mov_b64_e32 v[90:91], 0
	v_mov_b64_e32 v[92:93], 0
	v_mov_b64_e32 v[94:95], 0
	v_mov_b64_e32 v[96:97], 0
	v_mov_b64_e32 v[98:99], 0
	v_mov_b64_e32 v[100:101], 0
	v_mov_b64_e32 v[102:103], 0
	v_mov_b64_e32 v[104:105], 0
	v_mov_b64_e32 v[106:107], 0
	v_mov_b64_e32 v[108:109], 0
	v_mov_b64_e32 v[110:111], 0
	v_mov_b64_e32 v[112:113], 0
	v_mov_b64_e32 v[114:115], 0
	v_mov_b64_e32 v[116:117], 0
	v_mov_b64_e32 v[118:119], 0
	v_mov_b64_e32 v[120:121], 0
	v_mov_b64_e32 v[122:123], 0
	v_mov_b64_e32 v[124:125], 0
	v_mov_b64_e32 v[126:127], 0
	v_mov_b64_e32 v[128:129], 0

; template <class Epi, class Sched, bool ALIGN_EPI, bool SP2, bool FP8 = false>
; __device__ __forceinline__ void gemm_phase(LAS unsigned char* lds, const int K, const Sched& S, const Epi& E) {
;     ...
; #pragma unroll
;         for (int a = 0; a < 2; ++a)
; #pragma unroll
;             for (int b = 0; b < 2; ++b)
; #pragma unroll
;                 for (int m = 0; m < 4; ++m)
; #pragma unroll
;                     for (int n = 0; n < 2; ++n) acc[a][b][m][n] = (f32x4){0.f, 0.f, 0.f, 0.f};
;         cur = nxt; cA = nA; cB = nB; ++ui;
; #pragma unroll
;         for (int h = 0; h < 2; ++h)
; #pragma unroll
;             for (int i = 0; i < 2; ++i) vAc[h][i] = vAn[h][i];
.LBB0_1024:
	v_mov_b32_e32 v131, v159
	v_mov_b32_e32 v133, v159
	s_add_u32 s45, s50, 0x100
	v_mov_b32_e32 v34, 0
	v_lshl_add_u64 v[136:137], s[40:41], 0, v[132:133]
	v_lshl_add_u64 v[138:139], s[40:41], 0, v[130:131]
	s_addc_u32 s49, s51, 0
	s_mov_b32 s68, -2
	s_mov_b64 s[50:51], 0
	v_mov_b64_e32 v[2:3], 0
	v_mov_b64_e32 v[4:5], 0
	v_mov_b64_e32 v[6:7], 0
	v_mov_b64_e32 v[8:9], 0
	v_mov_b64_e32 v[10:11], 0
	v_mov_b64_e32 v[12:13], 0
	v_mov_b64_e32 v[14:15], 0
	v_mov_b64_e32 v[16:17], 0
	v_mov_b64_e32 v[18:19], 0
	v_mov_b64_e32 v[20:21], 0
	v_mov_b64_e32 v[22:23], 0
	v_mov_b64_e32 v[24:25], 0
	v_mov_b64_e32 v[26:27], 0
	v_mov_b64_e32 v[28:29], 0
	v_mov_b64_e32 v[30:31], 0
	v_mov_b64_e32 v[32:33], 0
	v_mov_b32_e32 v35, v34
	v_mov_b64_e32 v[36:37], 0
	v_mov_b64_e32 v[38:39], 0
	v_mov_b64_e32 v[40:41], 0
	v_mov_b64_e32 v[42:43], 0
	v_mov_b64_e32 v[44:45], 0
	v_mov_b64_e32 v[46:47], 0
	v_mov_b64_e32 v[48:49], 0
	v_mov_b64_e32 v[50:51], 0
	v_mov_b64_e32 v[52:53], 0
	v_mov_b64_e32 v[54:55], 0
	v_mov_b64_e32 v[56:57], 0
	v_mov_b64_e32 v[58:59], 0
	v_mov_b64_e32 v[60:61], 0
	v_mov_b64_e32 v[62:63], 0
	v_mov_b64_e32 v[64:65], 0
	v_mov_b64_e32 v[66:67], 0
	v_mov_b64_e32 v[68:69], 0
	v_mov_b64_e32 v[70:71], 0
	v_mov_b64_e32 v[72:73], 0
	v_mov_b64_e32 v[74:75], 0
	v_mov_b64_e32 v[76:77], 0
	v_mov_b64_e32 v[78:79], 0
	v_mov_b64_e32 v[80:81], 0
	v_mov_b64_e32 v[82:83], 0
	v_mov_b64_e32 v[84:85], 0
	v_mov_b64_e32 v[86:87], 0
	v_mov_b64_e32 v[88:89], 0
	v_mov_b64_e32 v[90:91], 0
	v_mov_b64_e32 v[92:93], 0
	v_mov_b64_e32 v[94:95], 0
	v_mov_b64_e32 v[96:97], 0
	v_mov_b64_e32 v[98:99], 0
	v_mov_b64_e32 v[100:101], 0
	v_mov_b64_e32 v[102:103], 0
	v_mov_b64_e32 v[104:105], 0
	v_mov_b64_e32 v[106:107], 0
	v_mov_b64_e32 v[108:109], 0
	v_mov_b64_e32 v[110:111], 0
	v_mov_b64_e32 v[112:113], 0
	v_mov_b64_e32 v[114:115], 0
	v_mov_b64_e32 v[116:117], 0
	v_mov_b64_e32 v[118:119], 0
	v_mov_b64_e32 v[120:121], 0
	v_mov_b64_e32 v[122:123], 0
	v_mov_b64_e32 v[124:125], 0
	v_mov_b64_e32 v[126:127], 0
	v_mov_b64_e32 v[128:129], 0
	s_waitcnt lgkmcnt(0)

; template <class Epi, class Sched, bool ALIGN_EPI, bool SP2, bool FP8 = false>
; __device__ __forceinline__ void gemm_phase(LAS unsigned char* lds, const int K, const Sched& S, const Epi& E) {
;     ...
; #pragma unroll
;         for (int a = 0; a < 2; ++a)
; #pragma unroll
;             for (int b = 0; b < 2; ++b)
; #pragma unroll
;                 for (int m = 0; m < 4; ++m)
; #pragma unroll
;                     for (int n = 0; n < 2; ++n) acc[a][b][m][n] = (f32x4){0.f, 0.f, 0.f, 0.f};
;         cur = nxt; cA = nA; cB = nB; ++ui;
; #pragma unroll
;         for (int h = 0; h < 2; ++h)
; #pragma unroll
;             for (int i = 0; i < 2; ++i) vAc[h][i] = vAn[h][i];
.LBB0_1188:
	v_mov_b32_e32 v171, v163
	v_mov_b32_e32 v173, v163
	s_add_u32 s43, s50, 0x100
	v_mov_b32_e32 v74, 0
	v_lshl_add_u64 v[176:177], s[18:19], 0, v[172:173]
	v_lshl_add_u64 v[178:179], s[18:19], 0, v[170:171]
	s_addc_u32 s45, s51, 0
	s_mov_b32 s47, -2
	s_mov_b64 s[50:51], 0
	v_mov_b64_e32 v[34:35], 0
	v_mov_b64_e32 v[36:37], 0
	v_mov_b64_e32 v[38:39], 0
	v_mov_b64_e32 v[40:41], 0
	v_mov_b64_e32 v[42:43], 0
	v_mov_b64_e32 v[44:45], 0
	v_mov_b64_e32 v[46:47], 0
	v_mov_b64_e32 v[48:49], 0
	v_mov_b64_e32 v[50:51], 0
	v_mov_b64_e32 v[52:53], 0
	v_mov_b64_e32 v[54:55], 0
	v_mov_b64_e32 v[56:57], 0
	v_mov_b64_e32 v[58:59], 0
	v_mov_b64_e32 v[60:61], 0
	v_mov_b64_e32 v[62:63], 0
	v_mov_b64_e32 v[64:65], 0
	v_mov_b64_e32 v[66:67], 0
	v_mov_b64_e32 v[68:69], 0
	v_mov_b64_e32 v[70:71], 0
	v_mov_b64_e32 v[72:73], 0
	v_mov_b32_e32 v75, v74
	v_mov_b64_e32 v[76:77], 0
	v_mov_b64_e32 v[78:79], 0
	v_mov_b64_e32 v[80:81], 0
	v_mov_b64_e32 v[82:83], 0
	v_mov_b64_e32 v[84:85], 0
	v_mov_b64_e32 v[86:87], 0
	v_mov_b64_e32 v[88:89], 0
	v_mov_b64_e32 v[90:91], 0
	v_mov_b64_e32 v[92:93], 0
	v_mov_b64_e32 v[94:95], 0
	v_mov_b64_e32 v[96:97], 0
	v_mov_b64_e32 v[98:99], 0
	v_mov_b64_e32 v[100:101], 0
	v_mov_b64_e32 v[102:103], 0
	v_mov_b64_e32 v[104:105], 0
	v_mov_b64_e32 v[106:107], 0
	v_mov_b64_e32 v[108:109], 0
	v_mov_b64_e32 v[110:111], 0
	v_mov_b64_e32 v[112:113], 0
	v_mov_b64_e32 v[114:115], 0
	v_mov_b64_e32 v[116:117], 0
	v_mov_b64_e32 v[118:119], 0
	v_mov_b64_e32 v[120:121], 0
	v_mov_b64_e32 v[122:123], 0
	v_mov_b64_e32 v[124:125], 0
	v_mov_b64_e32 v[126:127], 0
	v_mov_b64_e32 v[128:129], 0
	v_mov_b64_e32 v[130:131], 0
	v_mov_b64_e32 v[132:133], 0
	v_mov_b64_e32 v[134:135], 0
	v_mov_b64_e32 v[136:137], 0
	v_mov_b64_e32 v[138:139], 0
	v_mov_b64_e32 v[140:141], 0
	v_mov_b64_e32 v[142:143], 0
	v_mov_b64_e32 v[144:145], 0
	v_mov_b64_e32 v[146:147], 0
	v_mov_b64_e32 v[148:149], 0
	v_mov_b64_e32 v[150:151], 0
	v_mov_b64_e32 v[152:153], 0
	v_mov_b64_e32 v[154:155], 0
	v_mov_b64_e32 v[156:157], 0
	v_mov_b64_e32 v[158:159], 0
	v_mov_b64_e32 v[160:161], 0

; template <class Epi, class Sched, bool ALIGN_EPI, bool SP2, bool FP8 = false>
; __device__ __forceinline__ void gemm_phase(LAS unsigned char* lds, const int K, const Sched& S, const Epi& E) {
;     ...
; #pragma unroll
;         for (int a = 0; a < 2; ++a)
; #pragma unroll
;             for (int b = 0; b < 2; ++b)
; #pragma unroll
;                 for (int m = 0; m < 4; ++m)
; #pragma unroll
;                     for (int n = 0; n < 2; ++n) acc[a][b][m][n] = (f32x4){0.f, 0.f, 0.f, 0.f};
;         cur = nxt; cA = nA; cB = nB; ++ui;
; #pragma unroll
;         for (int h = 0; h < 2; ++h)
; #pragma unroll
;             for (int i = 0; i < 2; ++i) vAc[h][i] = vAn[h][i];
.LBB0_1328:
	v_mov_b32_e32 v171, v167
	v_mov_b32_e32 v175, v167
	s_add_u32 s41, s50, 0x100
	v_mov_b32_e32 v54, 0
	v_lshl_add_u64 v[178:179], s[16:17], 0, v[174:175]
	v_lshl_add_u64 v[180:181], s[16:17], 0, v[170:171]
	s_addc_u32 s43, s51, 0
	s_mov_b32 s49, -2
	s_mov_b64 s[50:51], 0
	v_mov_b64_e32 v[34:35], 0
	v_mov_b64_e32 v[36:37], 0
	v_mov_b64_e32 v[38:39], 0
	v_mov_b64_e32 v[40:41], 0
	v_mov_b64_e32 v[42:43], 0
	v_mov_b64_e32 v[44:45], 0
	v_mov_b64_e32 v[46:47], 0
	v_mov_b64_e32 v[48:49], 0
	v_mov_b64_e32 v[50:51], 0
	v_mov_b64_e32 v[52:53], 0
	v_mov_b32_e32 v55, v54
	v_mov_b64_e32 v[56:57], 0
	v_mov_b64_e32 v[58:59], 0
	v_mov_b64_e32 v[60:61], 0
	v_mov_b64_e32 v[62:63], 0
	v_mov_b64_e32 v[64:65], 0
	v_mov_b64_e32 v[66:67], 0
	v_mov_b64_e32 v[68:69], 0
	v_mov_b64_e32 v[70:71], 0
	v_mov_b64_e32 v[72:73], 0
	v_mov_b64_e32 v[74:75], 0
	v_mov_b64_e32 v[76:77], 0
	v_mov_b64_e32 v[78:79], 0
	v_mov_b64_e32 v[80:81], 0
	v_mov_b64_e32 v[82:83], 0
	v_mov_b64_e32 v[84:85], 0
	v_mov_b64_e32 v[86:87], 0
	v_mov_b64_e32 v[88:89], 0
	v_mov_b64_e32 v[90:91], 0
	v_mov_b64_e32 v[92:93], 0
	v_mov_b64_e32 v[94:95], 0
	v_mov_b64_e32 v[96:97], 0
	v_mov_b64_e32 v[98:99], 0
	v_mov_b64_e32 v[100:101], 0
	v_mov_b64_e32 v[102:103], 0
	v_mov_b64_e32 v[104:105], 0
	v_mov_b64_e32 v[106:107], 0
	v_mov_b64_e32 v[108:109], 0
	v_mov_b64_e32 v[110:111], 0
	v_mov_b64_e32 v[112:113], 0
	v_mov_b64_e32 v[114:115], 0
	v_mov_b64_e32 v[116:117], 0
	v_mov_b64_e32 v[118:119], 0
	v_mov_b64_e32 v[120:121], 0
	v_mov_b64_e32 v[122:123], 0
	v_mov_b64_e32 v[124:125], 0
	v_mov_b64_e32 v[126:127], 0
	v_mov_b64_e32 v[128:129], 0
	v_mov_b64_e32 v[130:131], 0
	v_mov_b64_e32 v[132:133], 0
	v_mov_b64_e32 v[134:135], 0
	v_mov_b64_e32 v[136:137], 0
	v_mov_b64_e32 v[138:139], 0
	v_mov_b64_e32 v[140:141], 0
	v_mov_b64_e32 v[142:143], 0
	v_mov_b64_e32 v[144:145], 0
	v_mov_b64_e32 v[146:147], 0
	v_mov_b64_e32 v[148:149], 0
	v_mov_b64_e32 v[150:151], 0
	v_mov_b64_e32 v[152:153], 0
	v_mov_b64_e32 v[154:155], 0
	v_mov_b64_e32 v[156:157], 0
	v_mov_b64_e32 v[158:159], 0
	v_mov_b64_e32 v[160:161], 0
